# v26 + accumulators zeroed by 4 f32 MFMAs (32x32x1_2b, zero operands) instead of 128 v_mov per unit in 8 GEMM loops
# baseline (speedup 1.0000x reference)
.LBB0_176:
	s_add_u32 s56, s26, 0x100
	s_addc_u32 s57, s27, 0
	v_mov_b32_e32 v167, v165
	v_mov_b32_e32 v169, v165
	s_add_u32 s58, s28, 0x100
	v_mfma_f32_32x32x1_2b_f32 v[32:63], v165, v165, 0
	v_mfma_f32_32x32x1_2b_f32 v[64:95], v165, v165, 0
	v_mfma_f32_32x32x1_2b_f32 v[96:127], v165, v165, 0
	v_mfma_f32_32x32x1_2b_f32 v[128:159], v165, v165, 0
	v_mov_b32_e32 v175, v165
	v_mov_b32_e32 v177, v165
	v_lshl_add_u64 v[178:179], s[16:17], 0, v[168:169]
	v_lshl_add_u64 v[180:181], s[16:17], 0, v[166:167]
	s_addc_u32 s59, s29, 0
	s_mov_b32 s60, -2
	s_mov_b64 s[26:27], 0
	s_branch .LBB0_178

.LBB0_589:
	s_lshl_b32 s4, s80, 10
	s_and_b32 s4, s4, 0x400
	s_add_u32 s27, s38, 0x100
	s_addc_u32 s86, s39, 0
	v_mov_b32_e32 v171, v165
	v_mov_b32_e32 v169, v165
	s_add_u32 s87, s40, 0x100
	v_mfma_f32_32x32x1_2b_f32 v[32:63], v165, v165, 0
	v_mfma_f32_32x32x1_2b_f32 v[64:95], v165, v165, 0
	v_mfma_f32_32x32x1_2b_f32 v[96:127], v165, v165, 0
	v_mfma_f32_32x32x1_2b_f32 v[128:159], v165, v165, 0
	v_add_u32_e32 v208, s4, v199
	v_lshl_add_u64 v[174:175], s[18:19], 0, v[168:169]
	v_lshl_add_u64 v[176:177], s[18:19], 0, v[170:171]
	s_addc_u32 s88, s41, 0
	s_mov_b32 s89, -2
	s_mov_b64 s[4:5], 0
	s_branch .LBB0_591

.LBB0_671:
	s_add_u32 s27, s34, 0x100
	s_addc_u32 s82, s35, 0
	v_mov_b32_e32 v167, v165
	v_mov_b32_e32 v169, v165
	s_add_u32 s83, s38, 0x100
	v_mfma_f32_32x32x1_2b_f32 v[32:63], v165, v165, 0
	v_mfma_f32_32x32x1_2b_f32 v[64:95], v165, v165, 0
	v_mfma_f32_32x32x1_2b_f32 v[96:127], v165, v165, 0
	v_mfma_f32_32x32x1_2b_f32 v[128:159], v165, v165, 0
	v_mov_b32_e32 v175, v165
	v_mov_b32_e32 v177, v165
	v_lshl_add_u64 v[178:179], s[16:17], 0, v[168:169]
	v_lshl_add_u64 v[180:181], s[16:17], 0, v[166:167]
	s_addc_u32 s84, s39, 0
	s_mov_b32 s85, -2
	s_mov_b64 s[34:35], 0
	s_branch .LBB0_673

.LBB0_816:
	s_add_u32 s56, s26, 0x100
	s_addc_u32 s57, s27, 0
	v_mov_b32_e32 v169, v165
	v_mov_b32_e32 v171, v165
	s_add_u32 s58, s28, 0x100
	v_mfma_f32_32x32x1_2b_f32 v[32:63], v165, v165, 0
	v_mfma_f32_32x32x1_2b_f32 v[64:95], v165, v165, 0
	v_mfma_f32_32x32x1_2b_f32 v[96:127], v165, v165, 0
	v_mfma_f32_32x32x1_2b_f32 v[128:159], v165, v165, 0
	v_mov_b32_e32 v175, v165
	v_mov_b32_e32 v177, v165
	v_lshl_add_u64 v[178:179], s[14:15], 0, v[170:171]
	v_lshl_add_u64 v[180:181], s[14:15], 0, v[168:169]
	s_addc_u32 s59, s29, 0
	s_mov_b32 s60, -2
	s_mov_b64 s[26:27], 0
	s_branch .LBB0_818

.LBB0_838:
	s_add_u32 s36, s4, 0x100
	s_addc_u32 s37, s5, 0
	v_mov_b32_e32 v129, v137
	v_mov_b32_e32 v131, v137
	s_add_u32 s57, s6, 0x100
	v_mfma_f32_32x32x1_2b_f32 v[0:31], v137, v137, 0
	v_mfma_f32_32x32x1_2b_f32 v[32:63], v137, v137, 0
	v_mfma_f32_32x32x1_2b_f32 v[64:95], v137, v137, 0
	v_mfma_f32_32x32x1_2b_f32 v[96:127], v137, v137, 0
	v_mov_b32_e32 v143, v137
	v_mov_b32_e32 v145, v137
	v_lshl_add_u64 v[146:147], s[22:23], 0, v[130:131]
	v_lshl_add_u64 v[148:149], s[22:23], 0, v[128:129]
	s_addc_u32 s60, s7, 0
	s_mov_b32 s61, -2
	s_mov_b64 s[4:5], 0
	s_branch .LBB0_840

.LBB0_1548:
	s_add_u32 s58, s24, 0x100
	s_addc_u32 s59, s25, 0
	v_mov_b32_e32 v169, v165
	v_mov_b32_e32 v171, v165
	s_add_u32 s60, s26, 0x100
	v_mfma_f32_32x32x1_2b_f32 v[32:63], v165, v165, 0
	v_mfma_f32_32x32x1_2b_f32 v[64:95], v165, v165, 0
	v_mfma_f32_32x32x1_2b_f32 v[96:127], v165, v165, 0
	v_mfma_f32_32x32x1_2b_f32 v[128:159], v165, v165, 0
	v_mov_b32_e32 v175, v165
	v_mov_b32_e32 v177, v165
	v_lshl_add_u64 v[178:179], s[14:15], 0, v[170:171]
	v_lshl_add_u64 v[180:181], s[14:15], 0, v[168:169]
	s_addc_u32 s61, s27, 0
	s_mov_b32 s62, -2
	s_mov_b64 s[24:25], 0
	s_waitcnt vmcnt(0)
	s_branch .LBB0_1550
